# baseline (speedup 1.0000x reference)
.LBB1_34:
	s_or_b64 exec, exec, s[12:13]
	v_xor_b32_e32 v44, 16, v38
	v_lshlrev_b32_e32 v44, 2, v44
	v_xor_b32_e32 v45, 32, v38
	v_lshlrev_b32_e32 v45, 2, v45
	s_mov_b32 s12, 0x99999999
	s_mov_b32 s13, 0x99999999
	v_mov_b32_dpp v41, v19 quad_perm:[1,0,3,2] row_mask:0xf bank_mask:0xf
	v_min_u32_e32 v42, v19, v41
	v_max_u32_e32 v43, v19, v41
	v_cndmask_b32_e64 v19, v43, v42, s[12:13]
	s_mov_b32 s12, 0xc3c3c3c3
	s_mov_b32 s13, 0xc3c3c3c3
	v_mov_b32_dpp v41, v19 quad_perm:[2,3,0,1] row_mask:0xf bank_mask:0xf
	v_min_u32_e32 v42, v19, v41
	v_max_u32_e32 v43, v19, v41
	v_cndmask_b32_e64 v19, v43, v42, s[12:13]
	s_mov_b32 s12, 0xa5a5a5a5
	s_mov_b32 s13, 0xa5a5a5a5
	v_mov_b32_dpp v41, v19 quad_perm:[1,0,3,2] row_mask:0xf bank_mask:0xf
	v_min_u32_e32 v42, v19, v41
	v_max_u32_e32 v43, v19, v41
	v_cndmask_b32_e64 v19, v43, v42, s[12:13]
	s_mov_b32 s12, 0xf00ff00f
	s_mov_b32 s13, 0xf00ff00f
	v_mov_b32_dpp v41, v19 row_shl:4 row_mask:0xf bank_mask:0x5
	v_mov_b32_dpp v41, v19 row_shr:4 row_mask:0xf bank_mask:0xa
	v_min_u32_e32 v42, v19, v41
	v_max_u32_e32 v43, v19, v41
	v_cndmask_b32_e64 v19, v43, v42, s[12:13]
	s_mov_b32 s12, 0xcc33cc33
	s_mov_b32 s13, 0xcc33cc33
	v_mov_b32_dpp v41, v19 quad_perm:[2,3,0,1] row_mask:0xf bank_mask:0xf
	v_min_u32_e32 v42, v19, v41
	v_max_u32_e32 v43, v19, v41
	v_cndmask_b32_e64 v19, v43, v42, s[12:13]
	s_mov_b32 s12, 0xaa55aa55
	s_mov_b32 s13, 0xaa55aa55
	v_mov_b32_dpp v41, v19 quad_perm:[1,0,3,2] row_mask:0xf bank_mask:0xf
	v_min_u32_e32 v42, v19, v41
	v_max_u32_e32 v43, v19, v41
	v_cndmask_b32_e64 v19, v43, v42, s[12:13]
	s_mov_b32 s12, 0xff0000ff
	s_mov_b32 s13, 0xff0000ff
	v_mov_b32_dpp v41, v19 row_shl:8 row_mask:0xf bank_mask:0x3
	v_mov_b32_dpp v41, v19 row_shr:8 row_mask:0xf bank_mask:0xc
	v_min_u32_e32 v42, v19, v41
	v_max_u32_e32 v43, v19, v41
	v_cndmask_b32_e64 v19, v43, v42, s[12:13]
	s_mov_b32 s12, 0xf0f00f0f
	s_mov_b32 s13, 0xf0f00f0f
	v_mov_b32_dpp v41, v19 row_shl:4 row_mask:0xf bank_mask:0x5
	v_mov_b32_dpp v41, v19 row_shr:4 row_mask:0xf bank_mask:0xa
	v_min_u32_e32 v42, v19, v41
	v_max_u32_e32 v43, v19, v41
	v_cndmask_b32_e64 v19, v43, v42, s[12:13]
	s_mov_b32 s12, 0xcccc3333
	s_mov_b32 s13, 0xcccc3333
	v_mov_b32_dpp v41, v19 quad_perm:[2,3,0,1] row_mask:0xf bank_mask:0xf
	v_min_u32_e32 v42, v19, v41
	v_max_u32_e32 v43, v19, v41
	v_cndmask_b32_e64 v19, v43, v42, s[12:13]
	s_mov_b32 s12, 0xaaaa5555
	s_mov_b32 s13, 0xaaaa5555
	v_mov_b32_dpp v41, v19 quad_perm:[1,0,3,2] row_mask:0xf bank_mask:0xf
	v_min_u32_e32 v42, v19, v41
	v_max_u32_e32 v43, v19, v41
	v_cndmask_b32_e64 v19, v43, v42, s[12:13]
	s_mov_b32 s12, 0xffff
	s_mov_b32 s13, 0xffff0000
	ds_bpermute_b32 v41, v44, v19
	s_waitcnt lgkmcnt(0)
	v_min_u32_e32 v42, v19, v41
	v_max_u32_e32 v43, v19, v41
	v_cndmask_b32_e64 v19, v43, v42, s[12:13]
	s_mov_b32 s12, 0xff00ff
	s_mov_b32 s13, 0xff00ff00
	v_mov_b32_dpp v41, v19 row_shl:8 row_mask:0xf bank_mask:0x3
	v_mov_b32_dpp v41, v19 row_shr:8 row_mask:0xf bank_mask:0xc
	v_min_u32_e32 v42, v19, v41
	v_max_u32_e32 v43, v19, v41
	v_cndmask_b32_e64 v19, v43, v42, s[12:13]
	s_mov_b32 s12, 0xf0f0f0f
	s_mov_b32 s13, 0xf0f0f0f0
	v_mov_b32_dpp v41, v19 row_shl:4 row_mask:0xf bank_mask:0x5
	v_mov_b32_dpp v41, v19 row_shr:4 row_mask:0xf bank_mask:0xa
	v_min_u32_e32 v42, v19, v41
	v_max_u32_e32 v43, v19, v41
	v_cndmask_b32_e64 v19, v43, v42, s[12:13]
	s_mov_b32 s12, 0x33333333
	s_mov_b32 s13, 0xcccccccc
	v_mov_b32_dpp v41, v19 quad_perm:[2,3,0,1] row_mask:0xf bank_mask:0xf
	v_min_u32_e32 v42, v19, v41
	v_max_u32_e32 v43, v19, v41
	v_cndmask_b32_e64 v19, v43, v42, s[12:13]
	s_mov_b32 s12, 0x55555555
	s_mov_b32 s13, 0xaaaaaaaa
	v_mov_b32_dpp v41, v19 quad_perm:[1,0,3,2] row_mask:0xf bank_mask:0xf
	v_min_u32_e32 v42, v19, v41
	v_max_u32_e32 v43, v19, v41
	v_cndmask_b32_e64 v19, v43, v42, s[12:13]
	s_mov_b32 s12, 0xffffffff
	s_mov_b32 s13, 0x0
	ds_bpermute_b32 v41, v45, v19
	s_waitcnt lgkmcnt(0)
	v_min_u32_e32 v42, v19, v41
	v_max_u32_e32 v43, v19, v41
	v_cndmask_b32_e64 v19, v43, v42, s[12:13]
	s_mov_b32 s12, 0xffff
	s_mov_b32 s13, 0xffff
	ds_bpermute_b32 v41, v44, v19
	s_waitcnt lgkmcnt(0)
	v_min_u32_e32 v42, v19, v41
	v_max_u32_e32 v43, v19, v41
	v_cndmask_b32_e64 v19, v43, v42, s[12:13]
	s_mov_b32 s12, 0xff00ff
	s_mov_b32 s13, 0xff00ff
	v_mov_b32_dpp v41, v19 row_shl:8 row_mask:0xf bank_mask:0x3
	v_mov_b32_dpp v41, v19 row_shr:8 row_mask:0xf bank_mask:0xc
	v_min_u32_e32 v42, v19, v41
	v_max_u32_e32 v43, v19, v41
	v_cndmask_b32_e64 v19, v43, v42, s[12:13]
	s_mov_b32 s12, 0xf0f0f0f
	s_mov_b32 s13, 0xf0f0f0f
	v_mov_b32_dpp v41, v19 row_shl:4 row_mask:0xf bank_mask:0x5
	v_mov_b32_dpp v41, v19 row_shr:4 row_mask:0xf bank_mask:0xa
	v_min_u32_e32 v42, v19, v41
	v_max_u32_e32 v43, v19, v41
	v_cndmask_b32_e64 v19, v43, v42, s[12:13]
	s_mov_b32 s12, 0x33333333
	s_mov_b32 s13, 0x33333333
	v_mov_b32_dpp v41, v19 quad_perm:[2,3,0,1] row_mask:0xf bank_mask:0xf
	v_min_u32_e32 v42, v19, v41
	v_max_u32_e32 v43, v19, v41
	v_cndmask_b32_e64 v19, v43, v42, s[12:13]
	s_mov_b32 s12, 0x55555555
	s_mov_b32 s13, 0x55555555
	v_mov_b32_dpp v41, v19 quad_perm:[1,0,3,2] row_mask:0xf bank_mask:0xf
	v_min_u32_e32 v42, v19, v41
	v_max_u32_e32 v43, v19, v41
	v_cndmask_b32_e64 v19, v43, v42, s[12:13]
	v_subrev_u32_e32 v42, 13, v38
	v_cmp_gt_u32_e64 s[12:13], 17, v42
	v_add_u32_e32 v43, 34, v38
	v_add_u32_e32 v44, 17, v38
	v_cmp_lt_u32_e64 s[14:15], 29, v38
	v_sub_u32_e32 v39, 46, v38
	s_nop 0
	v_cndmask_b32_e64 v43, v43, v44, s[14:15]
	v_cndmask_b32_e64 v43, v43, v42, s[12:13]
	v_and_b32_e32 v39, 63, v39
	v_lshlrev_b32_e32 v39, 2, v39
	v_lshlrev_b32_e32 v43, 2, v43
	v_mov_b32_e32 v40, v19
	ds_bpermute_b32 v41, v39, v40
	ds_bpermute_b32 v45, v43, v40
	v_lshl_or_b32 v39, s2, 2, v18
	s_movk_i32 s2, 0x3fd
	v_cmp_gt_i32_e64 s[2:3], s2, v39
	s_and_b64 s[2:3], s[10:11], s[2:3]
	s_and_b64 exec, exec, s[2:3]
	s_cbranch_execz .LBB1_38
	v_cmp_gt_u32_e64 s[2:3], 32, v38
	v_mov_b32_e32 v18, 0
	v_mov_b32_e32 v19, 0
	v_mov_b32_e32 v20, 0
	v_mov_b32_e32 v21, 0
	s_and_saveexec_b64 s[8:9], s[2:3]
	s_cbranch_execz .LBB1_37
	s_waitcnt lgkmcnt(0)
	v_mov_b32_e32 v42, v45
	v_mov_b32_e32 v18, 2
	s_nop 0
	v_lshlrev_b32_sdwa v19, v18, v42 dst_sel:DWORD dst_unused:UNUSED_PAD src0_sel:DWORD src1_sel:BYTE_0
	v_lshlrev_b32_sdwa v20, v18, v41 dst_sel:DWORD dst_unused:UNUSED_PAD src0_sel:DWORD src1_sel:BYTE_0
	ds_read_b32 v18, v19 offset:21504
	ds_read_b32 v20, v20 offset:21504
	v_lshrrev_b32_e32 v21, 8, v41
	v_lshrrev_b32_e32 v19, 8, v42
	v_cndmask_b32_e64 v21, 0, v21, s[12:13]
